# grid barrier between prologue and layer-0 residual removed; unreachable padding keeps all later code at its original addresses
# speedup vs baseline: 1.0012x; 1.0012x over previous
.LBB0_107:
	s_or_b64 exec, exec, s[4:5]
	s_branch .LBB0_173
	s_nop 0
	s_nop 0
	s_nop 0
	s_nop 0
	s_nop 0
	s_nop 0
	s_nop 0
	s_nop 0
	s_nop 0
	s_nop 0
	s_nop 0
	s_nop 0
	s_nop 0
	s_nop 0
	s_nop 0
	s_nop 0
	s_nop 0
	s_nop 0
	s_nop 0
	s_nop 0
	s_nop 0
	s_nop 0
	s_nop 0
	s_nop 0
	s_nop 0
	s_nop 0
	s_nop 0
	s_nop 0
	s_nop 0
	s_nop 0
	s_nop 0
	s_nop 0
	s_nop 0
	s_nop 0
	s_nop 0
	s_nop 0
	s_nop 0
	s_nop 0
	s_nop 0
	s_nop 0
	s_nop 0
	s_nop 0
	s_nop 0
	s_nop 0
	s_nop 0
	s_nop 0
	s_nop 0
	s_nop 0
	s_nop 0
	s_nop 0
	s_nop 0
	s_nop 0
	s_nop 0
	s_nop 0
	s_nop 0
	s_nop 0
	s_nop 0
	s_nop 0
	s_nop 0
	s_nop 0
	s_nop 0
	s_nop 0
	s_nop 0
	s_nop 0
	s_nop 0
	s_nop 0
	s_nop 0
	s_nop 0
	s_nop 0
	s_nop 0
	s_nop 0
	s_nop 0
	s_nop 0
	s_nop 0
	s_nop 0
	s_nop 0
	s_nop 0
	s_nop 0
	s_nop 0
	s_nop 0
	s_nop 0
	s_nop 0
	s_nop 0
	s_nop 0
	s_nop 0
	s_nop 0
	s_nop 0
	s_nop 0
	s_nop 0
	s_nop 0
	s_nop 0
	s_nop 0
	s_nop 0
	s_nop 0
	s_nop 0
	s_nop 0
	s_nop 0
	s_nop 0
	s_nop 0
	s_nop 0
	s_nop 0
	s_nop 0
	s_nop 0
	s_nop 0
	s_nop 0
	s_nop 0
	s_nop 0
	s_nop 0
	s_nop 0
	s_nop 0
	s_nop 0
	s_nop 0
	s_nop 0
	s_nop 0
	s_nop 0
	s_nop 0
	s_nop 0
	s_nop 0
	s_nop 0
	s_nop 0
	s_nop 0
	s_nop 0
	s_nop 0
	s_nop 0
	s_nop 0
	s_nop 0
	s_nop 0
	s_nop 0
	s_nop 0
	s_nop 0
	s_nop 0
	s_nop 0
	s_nop 0
	s_nop 0
	s_nop 0
	s_nop 0
	s_nop 0
	s_nop 0
	s_nop 0
	s_nop 0
	s_nop 0
	s_nop 0
	s_nop 0
	s_nop 0
	s_nop 0
	s_nop 0
	s_nop 0
	s_nop 0
	s_nop 0
	s_nop 0
	s_nop 0
	s_nop 0
	s_nop 0
	s_nop 0
	s_nop 0
	s_nop 0
	s_nop 0
	s_nop 0
	s_nop 0
	s_nop 0
	s_nop 0
	s_nop 0
	s_nop 0
	s_nop 0
	s_nop 0
	s_nop 0
	s_nop 0
	s_nop 0
	s_nop 0
	s_nop 0
	s_nop 0
	s_nop 0
	s_nop 0
	s_nop 0
	s_nop 0
	s_nop 0
	s_nop 0
	s_nop 0
	s_nop 0
	s_nop 0
	s_nop 0
	s_nop 0
	s_nop 0
	s_nop 0
	s_nop 0
	s_nop 0
	s_nop 0
	s_nop 0
	s_nop 0
	s_nop 0
	s_nop 0
	s_nop 0
	s_nop 0
	s_nop 0
	s_nop 0
	s_nop 0
	s_nop 0
	s_nop 0
	s_nop 0
	s_nop 0
	s_nop 0
	s_nop 0
	s_nop 0
	s_nop 0
	s_nop 0
	s_nop 0
	s_nop 0
	s_nop 0
	s_nop 0
	s_nop 0
	s_nop 0
	s_nop 0
	s_nop 0
	s_nop 0
	s_nop 0
	s_nop 0
	s_nop 0
	s_nop 0
	s_nop 0
	s_nop 0
	s_nop 0
	s_nop 0
	s_nop 0
	s_nop 0
	s_nop 0
	s_nop 0
	s_nop 0
	s_nop 0
	s_nop 0
	s_nop 0
	s_nop 0
	s_nop 0
	s_nop 0
	s_nop 0
	s_nop 0
	s_nop 0
	s_nop 0
	s_nop 0
	s_nop 0
	s_nop 0
	s_nop 0
	s_nop 0
	s_nop 0
	s_nop 0
	s_nop 0
	s_nop 0
	s_nop 0
	s_nop 0
	s_nop 0
	s_nop 0
	s_nop 0
	s_nop 0
	s_nop 0
	s_nop 0
	s_nop 0
	s_nop 0
	s_nop 0
	s_nop 0
	s_nop 0
	s_nop 0
	s_nop 0
	s_nop 0
	s_nop 0
	s_nop 0
	s_nop 0
	s_nop 0
	s_nop 0
	s_nop 0
	s_nop 0
	s_nop 0
	s_nop 0
	s_nop 0
	s_nop 0
	s_nop 0
	s_nop 0
	s_nop 0
	s_nop 0
	s_nop 0
	s_nop 0
	s_nop 0
	s_nop 0
	s_nop 0
	s_nop 0
	s_nop 0
	s_nop 0
	s_nop 0
	s_nop 0
	s_nop 0
	s_nop 0
	s_nop 0
	s_nop 0
	s_nop 0
	s_nop 0
	s_nop 0
	s_nop 0
	s_nop 0
	s_nop 0
	s_nop 0
	s_nop 0
	s_nop 0
	s_nop 0
	s_nop 0
	s_nop 0
	s_nop 0
	s_nop 0
	s_nop 0
	s_nop 0
	s_nop 0
	s_nop 0
	s_nop 0
	s_nop 0
	s_nop 0
	s_nop 0
	s_nop 0
	s_nop 0
	s_nop 0
	s_nop 0
	s_nop 0
	s_nop 0
	s_nop 0
	s_nop 0
	s_nop 0
	s_nop 0
	s_nop 0
	s_nop 0
	s_nop 0
	s_nop 0
	s_nop 0
	s_nop 0
	s_nop 0
	s_nop 0
	s_nop 0
	s_nop 0
	s_nop 0
	s_nop 0
	s_nop 0
	s_nop 0
	s_nop 0
	s_nop 0
	s_nop 0
	s_nop 0
	s_nop 0
	s_nop 0
	s_nop 0
	s_nop 0
	s_nop 0
	s_nop 0
	s_nop 0
	s_nop 0
	s_nop 0
	s_nop 0
	s_nop 0
	s_nop 0
	s_nop 0
	s_nop 0
	s_nop 0
	s_nop 0
	s_nop 0
	s_nop 0
	s_nop 0
	s_nop 0
	s_nop 0
	s_nop 0
	s_nop 0
	s_nop 0
	s_nop 0
	s_nop 0
	s_nop 0
	s_nop 0
	s_nop 0
	s_nop 0
	s_nop 0
	s_nop 0
	s_nop 0
	s_nop 0
	s_nop 0
	s_nop 0
	s_nop 0
	s_nop 0
	s_nop 0
	s_nop 0
	s_nop 0
	s_nop 0
	s_nop 0
	s_nop 0
	s_nop 0
	s_nop 0
	s_nop 0
	s_nop 0
	s_nop 0
	s_nop 0
	s_nop 0
	s_nop 0
	s_nop 0
	s_nop 0
	s_nop 0
	s_nop 0
	s_nop 0
	s_nop 0
	s_nop 0
	s_nop 0
	s_nop 0
	s_nop 0
	s_nop 0
	s_nop 0
	s_nop 0
	s_nop 0
	s_nop 0
	s_nop 0
	s_nop 0
	s_nop 0
	s_nop 0
	s_nop 0
	s_nop 0
	s_nop 0
	s_nop 0
	s_nop 0
	s_nop 0
	s_nop 0
	s_nop 0
	s_nop 0
	s_nop 0
	s_nop 0
	s_nop 0
	s_nop 0
	s_nop 0
	s_nop 0
	s_nop 0
	s_nop 0
	s_nop 0
	s_nop 0
	s_nop 0
	s_nop 0
	s_nop 0
	s_nop 0
	s_nop 0
	s_nop 0
	s_nop 0
	s_nop 0
	s_nop 0
	s_nop 0
	s_nop 0
	s_nop 0
	s_nop 0
	s_nop 0
	s_nop 0
	s_nop 0
	s_nop 0
	s_nop 0
	s_nop 0
	s_nop 0
	s_nop 0
	s_nop 0
	s_nop 0
	s_nop 0
	s_nop 0
	s_nop 0
	s_nop 0
	s_nop 0
	s_nop 0
	s_nop 0
	s_nop 0
	s_nop 0
	s_nop 0
	s_nop 0
	s_nop 0
	s_nop 0
	s_nop 0
	s_nop 0
	s_nop 0
	s_nop 0
	s_nop 0
	s_nop 0
	s_nop 0
	s_nop 0
	s_nop 0
	s_nop 0
	s_nop 0
	s_nop 0
	s_nop 0
	s_nop 0
	s_nop 0
	s_nop 0
	s_nop 0
	s_nop 0
	s_nop 0
	s_nop 0
	s_nop 0
	s_nop 0
	s_nop 0
	s_nop 0
	s_nop 0
	s_nop 0
	s_nop 0
	s_nop 0
	s_nop 0
	s_nop 0
	s_nop 0
	s_nop 0
	s_nop 0
	s_nop 0
	s_nop 0
	s_nop 0
	s_nop 0
	s_nop 0
	s_nop 0
	s_nop 0
	s_nop 0
	s_nop 0
	s_nop 0
	s_nop 0
	s_nop 0
	s_nop 0
	s_nop 0
	s_nop 0
	s_nop 0
	s_nop 0
	s_nop 0
	s_nop 0
	s_nop 0
	s_nop 0
	s_nop 0
	s_nop 0
	s_nop 0
	s_nop 0
	s_nop 0
	s_nop 0
	s_nop 0
	s_nop 0
	s_nop 0
	s_nop 0
	s_nop 0
	s_nop 0
	s_nop 0
	s_nop 0
	s_nop 0
	s_nop 0
	s_nop 0
	s_nop 0
	s_nop 0
	s_nop 0
	s_nop 0
	s_nop 0
	s_nop 0
	s_nop 0
	s_nop 0
	s_nop 0
	s_nop 0
	s_nop 0
	s_nop 0
	s_nop 0
	s_nop 0
	s_nop 0
	s_nop 0
	s_nop 0
	s_nop 0
	s_nop 0
	s_nop 0
	s_nop 0
	s_nop 0
	s_nop 0
	s_nop 0
	s_nop 0
	s_nop 0
	s_nop 0
	s_nop 0
	s_nop 0
	s_nop 0
	s_nop 0
	s_nop 0
	s_nop 0
	s_nop 0
	s_nop 0
	s_nop 0
	s_nop 0
	s_nop 0
	s_nop 0
	s_nop 0
	s_nop 0
	s_nop 0
	s_nop 0
	s_nop 0
	s_nop 0
	s_nop 0
	s_nop 0
	s_nop 0
	s_nop 0
	s_nop 0
	s_nop 0
	s_nop 0
	s_nop 0
	s_nop 0
	s_nop 0
	s_nop 0
	s_nop 0
	s_nop 0
	s_nop 0
	s_nop 0
	s_nop 0
	s_nop 0
	s_nop 0
	s_nop 0
	s_nop 0
	s_nop 0
	s_nop 0
	s_nop 0
	s_nop 0
	s_nop 0
	s_nop 0
	s_nop 0
	s_nop 0
	s_nop 0
	s_nop 0
	s_nop 0
	s_nop 0
	s_nop 0
	s_nop 0
	s_nop 0
	s_nop 0
	s_nop 0
	s_nop 0
	s_nop 0
	s_nop 0
	s_nop 0
	s_nop 0
	s_nop 0
	s_nop 0
	s_nop 0
	s_nop 0
	s_nop 0
	s_nop 0
	s_nop 0
	s_nop 0
	s_nop 0
	s_nop 0
	s_nop 0
	s_nop 0
	s_nop 0
	s_nop 0
	s_nop 0
	s_nop 0
	s_nop 0
	s_nop 0
	s_nop 0
	s_nop 0
	s_nop 0
	s_nop 0
	s_nop 0
	s_nop 0
	s_nop 0
	s_nop 0
	s_nop 0
	s_nop 0
	s_nop 0
	s_nop 0
	s_nop 0
	s_nop 0
	s_nop 0
	s_nop 0
	s_nop 0
	s_nop 0
	s_nop 0
	s_nop 0
	s_nop 0
	s_nop 0
	s_nop 0
	s_nop 0
	s_nop 0
	s_nop 0
	s_nop 0
	s_nop 0
	s_nop 0
	s_nop 0
	s_nop 0
	s_nop 0
	s_nop 0
	s_nop 0
	s_nop 0
	s_nop 0
	s_nop 0
	s_nop 0
